# attention row-max reduction reordered: the first QK accumulator is reduced before the second, alternating the two running maxima (hides the last QK MFMA's latency)
# speedup vs baseline: 1.0099x; 1.0099x over previous
.LBB0_726:
	v_add_u32_e64 v164, s18, v239
	s_add_i32 m0, s38, s30
	s_nop 0
	global_load_lds_dwordx4 v244, s[98:99]
	s_add_i32 m0, s22, s31
	s_nop 0
	global_load_lds_dwordx4 v245, s[98:99]
	s_add_u32 s98, s98, 0x20000
	s_addc_u32 s99, s99, 0
	s_nop 0
	ds_read_b64_tr_b16 v[190:191], v164 offset:24576
	ds_read_b64_tr_b16 v[192:193], v164 offset:25088
	s_waitcnt lgkmcnt(2)
	s_nop 0
	v_mfma_f32_32x32x16_bf16 v[48:63], v[158:161], v[110:113], v[48:63]
	v_add_f32_e32 v114, v80, v81
	v_add_f32_e32 v114, v82, v114
	v_add_f32_e32 v114, v83, v114
	v_add_f32_e32 v114, v84, v114
	v_add_f32_e64 v114, v85, v114
	v_cvt_pk_bf16_f32 v126, v80, v81
	v_cvt_pk_bf16_f32 v127, v82, v83
	ds_read_b64_tr_b16 v[186:187], v164 offset:28672
	ds_read_b64_tr_b16 v[188:189], v164 offset:29184
	v_mfma_f32_32x32x16_bf16 v[32:47], v[146:149], v[110:113], v[32:47]
	v_add_f32_e32 v80, v86, v114
	v_add_f32_e32 v80, v87, v80
	v_add_f32_e32 v80, v88, v80
	v_add_f32_e32 v80, v89, v80
	v_cvt_pk_bf16_f32 v128, v84, v85
	v_cvt_pk_bf16_f32 v129, v86, v87
	ds_read_b64_tr_b16 v[182:183], v164 offset:25600
	ds_read_b64_tr_b16 v[184:185], v164 offset:26112
	v_mfma_f32_32x32x16_bf16 v[48:63], v[154:157], v[106:109], v[48:63]
	v_add_f32_e32 v80, v90, v80
	v_add_f32_e32 v80, v91, v80
	v_add_f32_e32 v80, v92, v80
	v_add_f32_e32 v80, v93, v80
	v_cvt_pk_bf16_f32 v122, v88, v89
	v_cvt_pk_bf16_f32 v123, v90, v91
	ds_read_b64_tr_b16 v[178:179], v164 offset:29696
	ds_read_b64_tr_b16 v[180:181], v164 offset:30208
	v_mfma_f32_32x32x16_bf16 v[32:47], v[142:145], v[106:109], v[32:47]
	v_add_f32_e32 v80, v94, v80
	v_add_f32_e32 v80, v95, v80
	v_add_f32_e32 v80, v64, v80
	v_add_f32_e32 v80, v65, v80
	v_cvt_pk_bf16_f32 v124, v92, v93
	v_cvt_pk_bf16_f32 v125, v94, v95
	ds_read_b64_tr_b16 v[166:167], v164 offset:26624
	ds_read_b64_tr_b16 v[168:169], v164 offset:27136
	v_mfma_f32_32x32x16_bf16 v[48:63], v[150:153], v[102:105], v[48:63]
	v_add_f32_e32 v80, v66, v80
	v_add_f32_e32 v80, v67, v80
	v_add_f32_e32 v80, v68, v80
	v_add_f32_e32 v80, v69, v80
	v_cvt_pk_bf16_f32 v118, v64, v65
	v_cvt_pk_bf16_f32 v119, v66, v67
	ds_read_b64_tr_b16 v[174:175], v164 offset:30720
	ds_read_b64_tr_b16 v[176:177], v164 offset:31232
	v_mfma_f32_32x32x16_bf16 v[32:47], v[138:141], v[102:105], v[32:47]
	v_add_f32_e32 v64, v70, v80
	v_add_f32_e32 v64, v71, v64
	v_add_f32_e32 v64, v72, v64
	v_add_f32_e32 v64, v73, v64
	v_cvt_pk_bf16_f32 v120, v68, v69
	v_cvt_pk_bf16_f32 v121, v70, v71
	ds_read_b64_tr_b16 v[170:171], v164 offset:27648
	ds_read_b64_tr_b16 v[172:173], v164 offset:28160
	v_mfma_f32_32x32x16_bf16 v[48:63], v[134:137], v[98:101], v[48:63]
	v_add_f32_e32 v64, v74, v64
	v_add_f32_e32 v64, v75, v64
	v_add_f32_e32 v64, v76, v64
	v_add_f32_e32 v64, v77, v64
	v_cvt_pk_bf16_f32 v114, v72, v73
	v_cvt_pk_bf16_f32 v115, v74, v75
	ds_read_b64_tr_b16 v[162:163], v164 offset:31744
	ds_read_b64_tr_b16 v[164:165], v164 offset:32256
	v_mfma_f32_32x32x16_bf16 v[32:47], v[130:133], v[98:101], v[32:47]
	v_add_f32_e32 v64, v78, v64
	v_add_f32_e32 v64, v79, v64
	v_add_f32_e64 v224, v240, v64
	v_cvt_pk_bf16_f32 v116, v76, v77
	v_cvt_pk_bf16_f32 v117, v78, v79
	s_waitcnt lgkmcnt(14)
	s_nop 0
	ds_read_b128 v[64:67], v205
	ds_read_b128 v[68:71], v205 offset:32
	ds_read_b128 v[82:85], v205 offset:128
	ds_read_b128 v[86:89], v205 offset:160
	ds_read_b128 v[72:75], v205 offset:64
	ds_read_b128 v[76:79], v205 offset:96
	ds_read_b128 v[90:93], v205 offset:192
	ds_read_b128 v[138:141], v205 offset:224
	v_max_f32_e64 v80, v48, v49
	v_max3_f32 v81, v50, v51, v52
	v_max3_f32 v80, v80, v53, v54
	v_max3_f32 v81, v81, v55, v56
	v_max3_f32 v80, v80, v57, v58
	v_max3_f32 v81, v81, v59, v60
	v_max3_f32 v80, v80, v61, v62
	v_max3_f32 v81, v81, v63, v32
	v_max3_f32 v80, v80, v33, v34
	v_max3_f32 v81, v81, v35, v36
	v_max3_f32 v80, v80, v37, v38
	v_max3_f32 v81, v81, v39, v40
	v_max3_f32 v80, v80, v41, v42
	v_max3_f32 v81, v81, v43, v44
	v_max3_f32 v80, v80, v45, v46
	v_max3_f32 v80, v80, v47, v81
	v_mov_b32_e32 v81, v80
	s_nop 1
	v_permlane32_swap_b32_e32 v80, v81
	v_max_f32_e32 v80, v80, v81
	v_cmp_lt_f32_e32 vcc, s51, v80
	s_cmp_lg_u64 vcc, 0
	s_cselect_b64 s[18:19], -1, 0
	s_cbranch_vccnz .LBB0_734

.LBB0_729:
	s_add_i32 s18, s22, 0x2000
	v_add_u32_e64 v162, s38, v239
	s_cmpk_lg_i32 s22, 0x4000
	s_cselect_b32 s38, s18, 0
	s_add_i32 m0, s22, s30
	s_nop 0
	global_load_lds_dwordx4 v244, s[98:99]
	s_add_i32 m0, s38, s31
	s_nop 0
	global_load_lds_dwordx4 v245, s[98:99]
	s_add_u32 s98, s98, 0x20000
	s_addc_u32 s99, s99, 0
	s_nop 0
	ds_read_b64_tr_b16 v[194:195], v162 offset:24576
	ds_read_b64_tr_b16 v[196:197], v162 offset:25088
	s_waitcnt lgkmcnt(2)
	s_nop 0
	v_mfma_f32_32x32x16_bf16 v[80:95], v[134:137], v[110:113], v[80:95]
	v_add_f32_e32 v114, v48, v49
	v_add_f32_e32 v114, v50, v114
	v_add_f32_e32 v114, v51, v114
	v_add_f32_e32 v114, v52, v114
	v_add_f32_e64 v114, v53, v114
	v_cvt_pk_bf16_f32 v126, v48, v49
	v_cvt_pk_bf16_f32 v127, v50, v51
	ds_read_b64_tr_b16 v[190:191], v162 offset:28672
	ds_read_b64_tr_b16 v[192:193], v162 offset:29184
	v_mfma_f32_32x32x16_bf16 v[64:79], v[130:133], v[110:113], v[64:79]
	v_add_f32_e32 v48, v54, v114
	v_add_f32_e32 v48, v55, v48
	v_add_f32_e32 v48, v56, v48
	v_add_f32_e32 v48, v57, v48
	v_cvt_pk_bf16_f32 v128, v52, v53
	v_cvt_pk_bf16_f32 v129, v54, v55
	ds_read_b64_tr_b16 v[186:187], v162 offset:25600
	ds_read_b64_tr_b16 v[188:189], v162 offset:26112
	v_mfma_f32_32x32x16_bf16 v[80:95], v[146:149], v[106:109], v[80:95]
	v_add_f32_e32 v48, v58, v48
	v_add_f32_e32 v48, v59, v48
	v_add_f32_e32 v48, v60, v48
	v_add_f32_e32 v48, v61, v48
	v_cvt_pk_bf16_f32 v122, v56, v57
	v_cvt_pk_bf16_f32 v123, v58, v59
	ds_read_b64_tr_b16 v[138:139], v162 offset:29696
	ds_read_b64_tr_b16 v[140:141], v162 offset:30208
	v_mfma_f32_32x32x16_bf16 v[64:79], v[142:145], v[106:109], v[64:79]
	v_add_f32_e32 v48, v62, v48
	v_add_f32_e32 v48, v63, v48
	v_add_f32_e32 v48, v32, v48
	v_add_f32_e32 v48, v33, v48
	v_cvt_pk_bf16_f32 v124, v60, v61
	v_cvt_pk_bf16_f32 v125, v62, v63
	ds_read_b64_tr_b16 v[182:183], v162 offset:26624
	ds_read_b64_tr_b16 v[184:185], v162 offset:27136
	v_mfma_f32_32x32x16_bf16 v[80:95], v[158:161], v[102:105], v[80:95]
	v_add_f32_e32 v48, v34, v48
	v_add_f32_e32 v48, v35, v48
	v_add_f32_e32 v48, v36, v48
	v_add_f32_e32 v48, v37, v48
	v_cvt_pk_bf16_f32 v118, v32, v33
	v_cvt_pk_bf16_f32 v119, v34, v35
	ds_read_b64_tr_b16 v[178:179], v162 offset:30720
	ds_read_b64_tr_b16 v[180:181], v162 offset:31232
	v_mfma_f32_32x32x16_bf16 v[64:79], v[154:157], v[102:105], v[64:79]
	v_add_f32_e32 v32, v38, v48
	v_add_f32_e32 v32, v39, v32
	v_add_f32_e32 v32, v40, v32
	v_add_f32_e32 v32, v41, v32
	v_cvt_pk_bf16_f32 v120, v36, v37
	v_cvt_pk_bf16_f32 v121, v38, v39
	ds_read_b64_tr_b16 v[174:175], v162 offset:27648
	ds_read_b64_tr_b16 v[176:177], v162 offset:28160
	v_mfma_f32_32x32x16_bf16 v[80:95], v[166:169], v[98:101], v[80:95]
	v_add_f32_e32 v32, v42, v32
	v_add_f32_e32 v32, v43, v32
	v_add_f32_e32 v32, v44, v32
	v_add_f32_e32 v32, v45, v32
	v_cvt_pk_bf16_f32 v114, v40, v41
	v_cvt_pk_bf16_f32 v115, v42, v43
	ds_read_b64_tr_b16 v[170:171], v162 offset:31744
	ds_read_b64_tr_b16 v[172:173], v162 offset:32256
	v_mfma_f32_32x32x16_bf16 v[64:79], v[150:153], v[98:101], v[64:79]
	v_add_f32_e32 v32, v46, v32
	v_add_f32_e32 v32, v47, v32
	v_add_f32_e64 v240, v224, v32
	v_cvt_pk_bf16_f32 v116, v44, v45
	v_cvt_pk_bf16_f32 v117, v46, v47
	s_waitcnt lgkmcnt(14)
	s_nop 0
	ds_read_b128 v[32:35], v205 offset:256
	ds_read_b128 v[36:39], v205 offset:288
	ds_read_b128 v[50:53], v205 offset:384
	ds_read_b128 v[54:57], v205 offset:416
	ds_read_b128 v[40:43], v205 offset:320
	ds_read_b128 v[44:47], v205 offset:352
	ds_read_b128 v[58:61], v205 offset:448
	ds_read_b128 v[162:165], v205 offset:480
	v_max_f32_e64 v48, v80, v81
	v_max3_f32 v49, v82, v83, v84
	v_max3_f32 v48, v48, v85, v86
	v_max3_f32 v49, v49, v87, v88
	v_max3_f32 v48, v48, v89, v90
	v_max3_f32 v49, v49, v91, v92
	v_max3_f32 v48, v48, v93, v94
	v_max3_f32 v49, v49, v95, v64
	v_max3_f32 v48, v48, v65, v66
	v_max3_f32 v49, v49, v67, v68
	v_max3_f32 v48, v48, v69, v70
	v_max3_f32 v49, v49, v71, v72
	v_max3_f32 v48, v48, v73, v74
	v_max3_f32 v49, v49, v75, v76
	v_max3_f32 v48, v48, v77, v78
	v_max3_f32 v48, v48, v79, v49
	v_mov_b32_e32 v49, v48
	s_nop 1
	v_permlane32_swap_b32_e32 v48, v49
	v_max_f32_e32 v48, v48, v49
	v_cmp_lt_f32_e32 vcc, s51, v48
	s_cmp_lg_u64 vcc, 0
	s_cselect_b64 s[18:19], -1, 0
	s_cbranch_vccnz .LBB0_737
